# MLA attention loop: next tile's 5 LDS-DMA pieces issued one per MFMA gap behind the first QK MFMAs instead of back to back in front of them
# speedup vs baseline: 1.0260x; 1.0170x over previous
; template <bool MLA>
; __device__ __forceinline__ void attn_unit(char* lds, int h, int qb, const bf16_t* Qp, int ldq, const bf16_t* Kp, int ldk, const bf16_t* KRp, const bf16_t* Vp, int ldv,
;                                           unsigned char* Op, int ldo, const float* KMp, const float* rel_bias) {
;     ...
;             { const int vb0 = vrb + buf * SHM_V;
;     ...
;               PV_D0(0); PV_D0(1); PV_D0(2); PV_D0(3);
.LBB0_1384:
	v_add_f32_e32 v179, v83, v84
	v_fmac_f32_e32 v179, v178, v82
	v_add_u32_e32 v178, s53, v194
	ds_read_b64_tr_b16 v[82:83], v178 offset:0
	ds_read_b64_tr_b16 v[84:85], v178 offset:0x800
	ds_read_b64_tr_b16 v[86:87], v178 offset:0x1000
	ds_read_b64_tr_b16 v[88:89], v178 offset:0x1800
	ds_read_b64_tr_b16 v[90:91], v178 offset:0x2000
	ds_read_b64_tr_b16 v[92:93], v178 offset:0x2800
	ds_read_b64_tr_b16 v[94:95], v178 offset:0x3000
	ds_read_b64_tr_b16 v[96:97], v178 offset:0x3800
	s_waitcnt lgkmcnt(0)
	s_nop 0
	v_mfma_f32_32x32x16_bf16 v[34:49], v[66:69], v[82:85], v[34:49]
	v_mfma_f32_32x32x16_bf16 v[34:49], v[70:73], v[86:89], v[34:49]
	v_mfma_f32_32x32x16_bf16 v[34:49], v[74:77], v[90:93], v[34:49]
	v_mfma_f32_32x32x16_bf16 v[34:49], v[78:81], v[94:97], v[34:49]
	ds_read_b64_tr_b16 v[82:83], v178 offset:0x200
	ds_read_b64_tr_b16 v[84:85], v178 offset:0xa00
	ds_read_b64_tr_b16 v[86:87], v178 offset:0x1200
	ds_read_b64_tr_b16 v[88:89], v178 offset:0x1a00
	ds_read_b64_tr_b16 v[90:91], v178 offset:0x2200
	ds_read_b64_tr_b16 v[92:93], v178 offset:0x2a00
	ds_read_b64_tr_b16 v[94:95], v178 offset:0x3200
	ds_read_b64_tr_b16 v[96:97], v178 offset:0x3a00
	s_waitcnt lgkmcnt(0)
	s_nop 0
	v_mfma_f32_32x32x16_bf16 v[50:65], v[66:69], v[82:85], v[50:65]
	v_mfma_f32_32x32x16_bf16 v[50:65], v[70:73], v[86:89], v[50:65]
	v_mfma_f32_32x32x16_bf16 v[50:65], v[74:77], v[90:93], v[50:65]
	v_mfma_f32_32x32x16_bf16 v[50:65], v[78:81], v[94:97], v[50:65]
	ds_read_b64_tr_b16 v[82:83], v178 offset:0x400
	ds_read_b64_tr_b16 v[84:85], v178 offset:0xc00
	ds_read_b64_tr_b16 v[86:87], v178 offset:0x1400
	ds_read_b64_tr_b16 v[88:89], v178 offset:0x1c00
	ds_read_b64_tr_b16 v[90:91], v178 offset:0x2400
	ds_read_b64_tr_b16 v[92:93], v178 offset:0x2c00
	ds_read_b64_tr_b16 v[94:95], v178 offset:0x3400
	ds_read_b64_tr_b16 v[96:97], v178 offset:0x3c00
	s_waitcnt lgkmcnt(0)
	s_nop 0
	v_mfma_f32_32x32x16_bf16 v[18:33], v[66:69], v[82:85], v[18:33]
	v_mfma_f32_32x32x16_bf16 v[18:33], v[70:73], v[86:89], v[18:33]
	v_mfma_f32_32x32x16_bf16 v[18:33], v[74:77], v[90:93], v[18:33]
	v_mfma_f32_32x32x16_bf16 v[18:33], v[78:81], v[94:97], v[18:33]
	ds_read_b64_tr_b16 v[82:83], v178 offset:0x600
	ds_read_b64_tr_b16 v[84:85], v178 offset:0xe00
	ds_read_b64_tr_b16 v[86:87], v178 offset:0x1600
	ds_read_b64_tr_b16 v[88:89], v178 offset:0x1e00
	ds_read_b64_tr_b16 v[90:91], v178 offset:0x2600
	ds_read_b64_tr_b16 v[92:93], v178 offset:0x2e00
	ds_read_b64_tr_b16 v[94:95], v178 offset:0x3600
	ds_read_b64_tr_b16 v[96:97], v178 offset:0x3e00
	s_waitcnt lgkmcnt(0)
	s_nop 0
	v_mfma_f32_32x32x16_bf16 v[2:17], v[66:69], v[82:85], v[2:17]
	v_mfma_f32_32x32x16_bf16 v[2:17], v[70:73], v[86:89], v[2:17]
	v_mfma_f32_32x32x16_bf16 v[2:17], v[74:77], v[90:93], v[2:17]
	v_mfma_f32_32x32x16_bf16 v[2:17], v[78:81], v[94:97], v[2:17]
	v_mov_b32_e32 v178, v179
	s_branch .LBB0_1385
.Lmla_inact:
	s_cmp_ge_u32 s52, s50
	s_cbranch_scc1 .LBB0_1385
	s_lshl_b64 s[54:55], s[10:11], 12
	s_add_u32 s54, s44, s54
	s_addc_u32 s55, s45, s55
	s_lshl_b32 s22, s46, 14
	s_xor_b32 s22, s22, 0x4000
	s_add_i32 s22, s48, s22
	s_add_i32 m0, s22, 0x8000
	v_lshl_add_u64 v[66:67], v[146:147], 1, s[54:55]
	global_load_lds_dwordx4 v176, s[54:55]
	v_lshl_add_u64 v[68:69], v[66:67], 0, s[38:39]
	s_mov_b32 m0, s22
	v_lshl_add_u64 v[66:67], v[66:67], 0, s[40:41]
	global_load_lds_dwordx4 v[68:69], off
	s_add_i32 m0, s22, 0x8400
	s_nop 0
	global_load_lds_dwordx4 v177, s[54:55]
	s_add_i32 m0, s22, 0x400
	s_lshl_b32 s22, s46, 13
	s_lshl_b64 s[54:55], s[10:11], 7
	s_xor_b32 s22, s22, 0x2000
	global_load_lds_dwordx4 v[66:67], off
	v_lshl_add_u64 v[66:67], v[148:149], 0, s[54:55]
	s_add_i32 m0, s49, s22
	s_nop 0
	global_load_lds_dwordx4 v[66:67], off

; template <bool MLA>
; __device__ __forceinline__ void attn_unit(char* lds, int h, int qb, const bf16_t* Qp, int ldq, const bf16_t* Kp, int ldk, const bf16_t* KRp, const bf16_t* Vp, int ldv,
;                                           unsigned char* Op, int ldo, const float* KMp, const float* rel_bias) {
;     ...
;         if (t + 1 < NT) A_ISSUE(kb + 64, buf ^ 1);
;         int act;
;         if (MLA || jb == qb) act = (kb <= qlo + 31) ? 1 : 0; else act = __any((int)((mysel >> jb) & 1u)) ? 1 : 0;
;         act = __builtin_amdgcn_readfirstlane(act);
;         if (act) {
;             f32x16 p0, p1;
; #pragma unroll
;             for (int r = 0; r < 16; ++r) { p0[r] = 0.f; p1[r] = 0.f; }
;             { const char* kn = lds + buf * SHM_KN; const char* kr = lds + buf * SHM_KR;
; #pragma unroll
;               for (int d0 = 0; d0 < 8; ++d0) { const char* ap = kn + kan[d0 & 3] + (d0 >> 2) * 128;
;                   const bf16x8 a0 = *(const bf16x8*)ap, a1 = *(const bf16x8*)(ap + 32 * 256);
;                   p0 = __builtin_amdgcn_mfma_f32_32x32x16_bf16(a0, qr[d0], p0, 0, 0, 0);
;                   p1 = __builtin_amdgcn_mfma_f32_32x32x16_bf16(a1, qr[d0], p1, 0, 0, 0); }
;               if constexpr (MLA) {
; #pragma unroll
;                   for (int d0 = 8; d0 < 12; ++d0) { const char* ap = kr + kar[d0 & 3];
;                       const bf16x8 a0 = *(const bf16x8*)ap, a1 = *(const bf16x8*)(ap + 32 * 128);
;                       p0 = __builtin_amdgcn_mfma_f32_32x32x16_bf16(a0, qr[d0], p0, 0, 0, 0);
;                       p1 = __builtin_amdgcn_mfma_f32_32x32x16_bf16(a1, qr[d0], p1, 0, 0, 0); } } }
.LBB0_1388:
	s_sub_i32 s22, s10, 64
	s_cmp_le_u32 s22, s51
	s_cselect_b64 s[54:55], -1, 0
	v_cndmask_b32_e64 v66, 0, 1, s[54:55]
	s_nop 0
	v_readfirstlane_b32 s22, v66
	s_bitcmp0_b32 s22, 0
	s_cbranch_scc1 .Lmla_inact
	s_lshl_b32 s53, s46, 14
	s_add_i32 s22, s53, 0
	v_add3_u32 v70, s22, v154, v153
	ds_read_b128 v[66:69], v70 offset:32768
	ds_read_b128 v[180:183], v70 offset:32896
	v_add3_u32 v179, s22, v155, v153
	s_lshl_b32 s23, s46, 13
	s_waitcnt lgkmcnt(0)
	v_mfma_f32_32x32x16_bf16 v[82:97], v[66:69], v[98:101], 0
	s_cmp_lt_u32 s52, s50
	s_cselect_b32 s101, 1, 0
	s_cbranch_scc0 .Lmla_nk0
	s_lshl_b64 s[98:99], s[10:11], 12
	s_add_u32 s98, s44, s98
	s_addc_u32 s99, s45, s99
	s_lshl_b32 s100, s46, 14
	s_xor_b32 s100, s100, 0x4000
	s_add_i32 s100, s48, s100
	s_add_i32 m0, s100, 0x8000
	v_lshl_add_u64 v[228:229], v[146:147], 1, s[98:99]
	global_load_lds_dwordx4 v176, s[98:99]
.Lmla_nk0:
	ds_read_b128 v[66:69], v70 offset:40960
	ds_read_b128 v[196:199], v70 offset:41088
	ds_read_b128 v[200:203], v179 offset:32768
	ds_read_b128 v[204:207], v179 offset:32896
	s_waitcnt lgkmcnt(0)
	v_mfma_f32_32x32x16_bf16 v[66:81], v[66:69], v[98:101], 0
	v_mfma_f32_32x32x16_bf16 v[82:97], v[200:203], v[102:105], v[82:97]
	s_cmp_lg_u32 s101, 0
	s_cbranch_scc0 .Lmla_nk1
	v_lshl_add_u64 v[230:231], v[228:229], 0, s[38:39]
	s_mov_b32 m0, s100
	v_lshl_add_u64 v[228:229], v[228:229], 0, s[40:41]
	global_load_lds_dwordx4 v[230:231], off
.Lmla_nk1:
	ds_read_b128 v[200:203], v179 offset:40960
	ds_read_b128 v[208:211], v179 offset:41088
	v_add3_u32 v179, s22, v156, v153
	s_waitcnt lgkmcnt(0)
	v_mfma_f32_32x32x16_bf16 v[66:81], v[200:203], v[102:105], v[66:81]
	s_cmp_lg_u32 s101, 0
	s_cbranch_scc0 .Lmla_nk2
	s_add_i32 m0, s100, 0x8400
	s_nop 0
	global_load_lds_dwordx4 v177, s[98:99]
.Lmla_nk2:
	ds_read_b128 v[200:203], v179 offset:32768
	ds_read_b128 v[212:215], v179 offset:32896
	s_waitcnt lgkmcnt(0)
	v_mfma_f32_32x32x16_bf16 v[82:97], v[200:203], v[106:109], v[82:97]
	s_cmp_lg_u32 s101, 0
	s_cbranch_scc0 .Lmla_nk3
	s_add_i32 m0, s100, 0x400
	s_nop 0
	global_load_lds_dwordx4 v[228:229], off
.Lmla_nk3:
	ds_read_b128 v[200:203], v179 offset:40960
	ds_read_b128 v[216:219], v179 offset:41088
	v_add3_u32 v179, s22, v157, v153
	s_sub_i32 s22, s22, s23
	s_waitcnt lgkmcnt(0)
	v_mfma_f32_32x32x16_bf16 v[66:81], v[200:203], v[106:109], v[66:81]
	s_cmp_lg_u32 s101, 0
	s_cbranch_scc0 .Lmla_nk4
	s_lshl_b32 s100, s46, 13
	s_lshl_b64 s[98:99], s[10:11], 7
	s_xor_b32 s100, s100, 0x2000
	v_lshl_add_u64 v[228:229], v[148:149], 0, s[98:99]
	s_add_i32 m0, s49, s100
	s_nop 0
	global_load_lds_dwordx4 v[228:229], off
; template <bool MLA>
; __device__ __forceinline__ void attn_unit(char* lds, int h, int qb, const bf16_t* Qp, int ldq, const bf16_t* Kp, int ldk, const bf16_t* KRp, const bf16_t* Vp, int ldv,
;                                           unsigned char* Op, int ldo, const float* KMp, const float* rel_bias) {
;     ...
;               for (int d0 = 0; d0 < 8; ++d0) { const char* ap = kn + kan[d0 & 3] + (d0 >> 2) * 128;
;                   const bf16x8 a0 = *(const bf16x8*)ap, a1 = *(const bf16x8*)(ap + 32 * 256);
;                   p0 = __builtin_amdgcn_mfma_f32_32x32x16_bf16(a0, qr[d0], p0, 0, 0, 0);
;                   p1 = __builtin_amdgcn_mfma_f32_32x32x16_bf16(a1, qr[d0], p1, 0, 0, 0); }
;               if constexpr (MLA) {
; #pragma unroll
;                   for (int d0 = 8; d0 < 12; ++d0) { const char* ap = kr + kar[d0 & 3];
;                       const bf16x8 a0 = *(const bf16x8*)ap, a1 = *(const bf16x8*)(ap + 32 * 128);
;                       p0 = __builtin_amdgcn_mfma_f32_32x32x16_bf16(a0, qr[d0], p0, 0, 0, 0);
;                       p1 = __builtin_amdgcn_mfma_f32_32x32x16_bf16(a1, qr[d0], p1, 0, 0, 0); } } }
;             const int dq = qpos - kb - 4 * hi;
;             if constexpr (MLA) {
;                 if (kb + 63 > qlo) {
; #pragma unroll
;                     for (int r = 0; r < 16; ++r) { const int d0 = dq - CROWC(r); if (d0 < 0) p0[r] = NEG; if (d0 < 32) p1[r] = NEG; } }
.Lmla_nk4:
	ds_read_b128 v[200:203], v179 offset:32768
	ds_read_b128 v[220:223], v179 offset:32896
	s_waitcnt lgkmcnt(0)
	v_mfma_f32_32x32x16_bf16 v[82:97], v[200:203], v[110:113], v[82:97]
	ds_read_b128 v[200:203], v179 offset:40960
	ds_read_b128 v[224:227], v179 offset:41088
	v_add3_u32 v179, s22, v154, v159
	s_waitcnt lgkmcnt(0)
	v_mfma_f32_32x32x16_bf16 v[66:81], v[200:203], v[110:113], v[66:81]
	v_mfma_f32_32x32x16_bf16 v[82:97], v[180:183], v[114:117], v[82:97]
	v_mfma_f32_32x32x16_bf16 v[66:81], v[196:199], v[114:117], v[66:81]
	ds_read_b128 v[180:183], v179
	ds_read_b128 v[196:199], v179 offset:4096
	v_add3_u32 v179, s22, v155, v159
	v_mfma_f32_32x32x16_bf16 v[82:97], v[204:207], v[118:121], v[82:97]
	v_mfma_f32_32x32x16_bf16 v[66:81], v[208:211], v[118:121], v[66:81]
	v_mfma_f32_32x32x16_bf16 v[82:97], v[212:215], v[122:125], v[82:97]
	v_mfma_f32_32x32x16_bf16 v[66:81], v[216:219], v[122:125], v[66:81]
	v_mfma_f32_32x32x16_bf16 v[82:97], v[220:223], v[126:129], v[82:97]
	v_mfma_f32_32x32x16_bf16 v[66:81], v[224:227], v[126:129], v[66:81]
	s_waitcnt lgkmcnt(0)
	v_mfma_f32_32x32x16_bf16 v[82:97], v[180:183], v[130:133], v[82:97]
	v_mfma_f32_32x32x16_bf16 v[66:81], v[196:199], v[130:133], v[66:81]
	ds_read_b128 v[180:183], v179
	ds_read_b128 v[196:199], v179 offset:4096
	v_add3_u32 v179, s22, v156, v159
	s_waitcnt lgkmcnt(0)
	v_mfma_f32_32x32x16_bf16 v[82:97], v[180:183], v[134:137], v[82:97]
	v_mfma_f32_32x32x16_bf16 v[66:81], v[196:199], v[134:137], v[66:81]
	ds_read_b128 v[180:183], v179
	ds_read_b128 v[196:199], v179 offset:4096
	v_add3_u32 v179, s22, v157, v159
	s_add_i32 s22, s10, -1
	s_cmp_le_u32 s22, s42
	s_waitcnt lgkmcnt(0)
	v_mfma_f32_32x32x16_bf16 v[82:97], v[180:183], v[138:141], v[82:97]
	v_mfma_f32_32x32x16_bf16 v[66:81], v[196:199], v[138:141], v[66:81]
	ds_read_b128 v[180:183], v179
	ds_read_b128 v[196:199], v179 offset:4096
	s_waitcnt lgkmcnt(0)
	v_mfma_f32_32x32x16_bf16 v[82:97], v[180:183], v[142:145], v[82:97]
	v_mfma_f32_32x32x16_bf16 v[66:81], v[196:199], v[142:145], v[66:81]
	s_cbranch_scc1 .LBB0_1391
	v_add_u32_e32 v179, 27, v174
	v_cmp_lt_i32_e32 vcc, -1, v179
	s_nop 7
	v_cndmask_b32_e32 v82, v163, v82, vcc
	v_cmp_lt_i32_e32 vcc, 31, v179
	v_add_u32_e32 v179, 26, v174
	s_nop 0
	v_cndmask_b32_e32 v66, v163, v66, vcc
	v_cmp_lt_i32_e32 vcc, -1, v179
	s_nop 1
	v_cndmask_b32_e32 v83, v163, v83, vcc
	v_cmp_lt_i32_e32 vcc, 31, v179
	v_add_u32_e32 v179, 25, v174
	s_nop 0
	v_cndmask_b32_e32 v67, v163, v67, vcc
	v_cmp_lt_i32_e32 vcc, -1, v179
	s_nop 1
	v_cndmask_b32_e32 v84, v163, v84, vcc
	v_cmp_lt_i32_e32 vcc, 31, v179
	v_add_u32_e32 v179, 24, v174
	s_nop 0
	v_cndmask_b32_e32 v68, v163, v68, vcc
	v_cmp_lt_i32_e32 vcc, -1, v179
	s_nop 1
	v_cndmask_b32_e32 v85, v163, v85, vcc
	v_cmp_lt_i32_e32 vcc, 31, v179
	v_add_u32_e32 v179, 19, v174
	s_nop 0
	v_cndmask_b32_e32 v69, v163, v69, vcc
	v_cmp_lt_i32_e32 vcc, -1, v179
	s_nop 1
	v_cndmask_b32_e32 v86, v163, v86, vcc
	v_cmp_lt_i32_e32 vcc, 31, v179
	v_add_u32_e32 v179, 18, v174
	s_nop 0
	v_cndmask_b32_e32 v70, v163, v70, vcc
	v_cmp_lt_i32_e32 vcc, -1, v179
	s_nop 1
	v_cndmask_b32_e32 v87, v163, v87, vcc
	v_cmp_lt_i32_e32 vcc, 31, v179
	v_add_u32_e32 v179, 17, v174
	s_nop 0
	v_cndmask_b32_e32 v71, v163, v71, vcc
	v_cmp_lt_i32_e32 vcc, -1, v179
	s_nop 1
	v_cndmask_b32_e32 v88, v163, v88, vcc
	v_cmp_lt_i32_e32 vcc, 31, v179
	v_add_u32_e32 v179, 16, v174
	s_nop 0
	v_cndmask_b32_e32 v72, v163, v72, vcc
	v_cmp_lt_i32_e32 vcc, -1, v179
	s_nop 1
	v_cndmask_b32_e32 v89, v163, v89, vcc
	v_cmp_lt_i32_e32 vcc, 31, v179
	v_add_u32_e32 v179, 11, v174
	s_nop 0
	v_cndmask_b32_e32 v73, v163, v73, vcc
	v_cmp_lt_i32_e32 vcc, -1, v179
	s_nop 1
	v_cndmask_b32_e32 v90, v163, v90, vcc
	v_cmp_lt_i32_e32 vcc, 31, v179
	v_add_u32_e32 v179, 10, v174
	s_nop 0
	v_cndmask_b32_e32 v74, v163, v74, vcc
	v_cmp_lt_i32_e32 vcc, -1, v179
	s_nop 1
	v_cndmask_b32_e32 v91, v163, v91, vcc
	v_cmp_lt_i32_e32 vcc, 31, v179
	v_add_u32_e32 v179, 9, v174
	s_nop 0
	v_cndmask_b32_e32 v75, v163, v75, vcc
	v_cmp_lt_i32_e32 vcc, -1, v179
	s_nop 1
	v_cndmask_b32_e32 v92, v163, v92, vcc
	v_cmp_lt_i32_e32 vcc, 31, v179
	v_add_u32_e32 v179, 8, v174
	s_nop 0
	v_cndmask_b32_e32 v76, v163, v76, vcc
	v_cmp_lt_i32_e32 vcc, -1, v179
	s_nop 1
	v_cndmask_b32_e32 v93, v163, v93, vcc
	v_cmp_lt_i32_e32 vcc, 31, v179
	v_add_u32_e32 v179, 3, v174
	s_nop 0
	v_cndmask_b32_e32 v77, v163, v77, vcc
	v_cmp_lt_i32_e32 vcc, -1, v179
	s_nop 1
	v_cndmask_b32_e32 v94, v163, v94, vcc
	v_cmp_lt_i32_e32 vcc, 31, v179
	v_add_u32_e32 v179, 2, v174
	s_nop 0
	v_cndmask_b32_e32 v78, v163, v78, vcc
	v_cmp_lt_i32_e32 vcc, -1, v179
	s_nop 1
	v_cndmask_b32_e32 v95, v163, v95, vcc
	v_cmp_lt_i32_e32 vcc, 31, v179
	v_add_u32_e32 v179, 1, v174
	s_nop 0
	v_cndmask_b32_e32 v79, v163, v79, vcc
	v_cmp_lt_i32_e32 vcc, -1, v179
	s_nop 1
	v_cndmask_b32_e32 v96, v163, v96, vcc
	v_cmp_lt_i32_e32 vcc, 31, v179
	s_nop 1
	v_cndmask_b32_e32 v80, v163, v80, vcc
	v_cmp_lt_i32_e32 vcc, -1, v174
	s_nop 1
	v_cndmask_b32_e32 v97, v163, v97, vcc
	v_cmp_lt_i32_e32 vcc, 31, v174
	s_nop 1
	v_cndmask_b32_e32 v81, v163, v81, vcc
